# gates GEMM epilogue: bias loads hoisted to unit start into dead VGPRs, vmcnt(0) drain removed
# baseline (speedup 1.0000x reference)
.LBB0_1975:
	s_lshl_b32 s100, s19, 8
	s_add_i32 s100, s100, 0xffffee00
	s_lshl_b32 s100, s100, 2
	s_add_u32 s100, s54, s100
	s_addc_u32 s101, s55, 0
	v_bfe_u32 v235, v162, 4, 2
	v_lshlrev_b32_e32 v235, 5, v235
	s_nop 1
	global_load_dwordx4 v[236:239], v235, s[100:101]
	global_load_dwordx4 v[240:243], v235, s[100:101] offset:16
	global_load_dwordx4 v[244:247], v235, s[100:101] offset:512
	global_load_dwordx4 v[248:251], v235, s[100:101] offset:528
	s_lshl_b32 s38, s57, 10
	s_and_b32 s38, s38, 0x400
	s_add_i32 s59, s38, 0
	s_lshl_b32 s21, s20, 8
	s_add_i32 s59, s59, 0x20000
	s_add_u32 s34, s34, 0x40080
	s_addc_u32 s35, s35, 0
	s_add_u32 s62, s36, 0x100
	v_mov_b32_e32 v4, 0
	s_addc_u32 s63, s37, 0
	s_mov_b32 s64, -2
	v_mov_b32_e32 v5, v4
	v_mov_b32_e32 v6, v4
	v_mov_b32_e32 v7, v4
	v_mov_b32_e32 v8, v4
	v_mov_b32_e32 v9, v4
	v_mov_b32_e32 v10, v4
	v_mov_b32_e32 v11, v4
	v_mov_b32_e32 v20, v4
	v_mov_b32_e32 v21, v4
	v_mov_b32_e32 v22, v4
	v_mov_b32_e32 v23, v4
	v_mov_b32_e32 v24, v4
	v_mov_b32_e32 v25, v4
	v_mov_b32_e32 v26, v4
	v_mov_b32_e32 v27, v4
	v_mov_b32_e32 v36, v4
	v_mov_b32_e32 v37, v4
	v_mov_b32_e32 v38, v4
	v_mov_b32_e32 v39, v4
	v_mov_b32_e32 v40, v4
	v_mov_b32_e32 v41, v4
	v_mov_b32_e32 v42, v4
	v_mov_b32_e32 v43, v4
	v_mov_b32_e32 v52, v4
	v_mov_b32_e32 v53, v4
	v_mov_b32_e32 v54, v4
	v_mov_b32_e32 v55, v4
	v_mov_b32_e32 v56, v4
	v_mov_b32_e32 v57, v4
	v_mov_b32_e32 v58, v4
	v_mov_b32_e32 v59, v4
	v_mov_b32_e32 v12, v4
	v_mov_b32_e32 v13, v4
	v_mov_b32_e32 v14, v4
	v_mov_b32_e32 v15, v4
	v_mov_b32_e32 v16, v4
	v_mov_b32_e32 v17, v4
	v_mov_b32_e32 v18, v4
	v_mov_b32_e32 v19, v4
	v_mov_b32_e32 v28, v4
	v_mov_b32_e32 v29, v4
	v_mov_b32_e32 v30, v4
	v_mov_b32_e32 v31, v4
	v_mov_b32_e32 v32, v4
	v_mov_b32_e32 v33, v4
	v_mov_b32_e32 v34, v4
	v_mov_b32_e32 v35, v4
	v_mov_b32_e32 v44, v4
	v_mov_b32_e32 v45, v4
	v_mov_b32_e32 v46, v4
	v_mov_b32_e32 v47, v4
	v_mov_b32_e32 v48, v4
	v_mov_b32_e32 v49, v4
	v_mov_b32_e32 v50, v4
	v_mov_b32_e32 v51, v4
	v_mov_b32_e32 v60, v4
	v_mov_b32_e32 v61, v4
	v_mov_b32_e32 v62, v4
	v_mov_b32_e32 v63, v4
	v_mov_b32_e32 v64, v4
	v_mov_b32_e32 v65, v4
	v_mov_b32_e32 v66, v4
	v_mov_b32_e32 v67, v4
	v_mov_b32_e32 v68, v4
	v_mov_b32_e32 v69, v4
	v_mov_b32_e32 v70, v4
	v_mov_b32_e32 v71, v4
	v_mov_b32_e32 v72, v4
	v_mov_b32_e32 v73, v4
	v_mov_b32_e32 v74, v4
	v_mov_b32_e32 v75, v4
	v_mov_b32_e32 v84, v4
	v_mov_b32_e32 v85, v4
	v_mov_b32_e32 v86, v4
	v_mov_b32_e32 v87, v4
	v_mov_b32_e32 v88, v4
	v_mov_b32_e32 v89, v4
	v_mov_b32_e32 v90, v4
	v_mov_b32_e32 v91, v4
	v_mov_b32_e32 v100, v4
	v_mov_b32_e32 v101, v4
	v_mov_b32_e32 v102, v4
	v_mov_b32_e32 v103, v4
	v_mov_b32_e32 v104, v4
	v_mov_b32_e32 v105, v4
	v_mov_b32_e32 v106, v4
	v_mov_b32_e32 v107, v4
	v_mov_b32_e32 v116, v4
	v_mov_b32_e32 v117, v4
	v_mov_b32_e32 v118, v4
	v_mov_b32_e32 v119, v4
	v_mov_b32_e32 v120, v4
	v_mov_b32_e32 v121, v4
	v_mov_b32_e32 v122, v4
	v_mov_b32_e32 v123, v4
	v_mov_b32_e32 v76, v4
	v_mov_b32_e32 v77, v4
	v_mov_b32_e32 v78, v4
	v_mov_b32_e32 v79, v4
	v_mov_b32_e32 v80, v4
	v_mov_b32_e32 v81, v4
	v_mov_b32_e32 v82, v4
	v_mov_b32_e32 v83, v4
	v_mov_b32_e32 v92, v4
	v_mov_b32_e32 v93, v4
	v_mov_b32_e32 v94, v4
	v_mov_b32_e32 v95, v4
	v_mov_b32_e32 v96, v4
	v_mov_b32_e32 v97, v4
	v_mov_b32_e32 v98, v4
	v_mov_b32_e32 v99, v4
	v_mov_b32_e32 v108, v4
	v_mov_b32_e32 v109, v4
	v_mov_b32_e32 v110, v4
	v_mov_b32_e32 v111, v4
	v_mov_b32_e32 v112, v4
	v_mov_b32_e32 v113, v4
	v_mov_b32_e32 v114, v4
	v_mov_b32_e32 v115, v4
	v_mov_b32_e32 v124, v4
	v_mov_b32_e32 v125, v4
	v_mov_b32_e32 v126, v4
	v_mov_b32_e32 v127, v4
	v_mov_b32_e32 v128, v4
	v_mov_b32_e32 v129, v4
	v_mov_b32_e32 v130, v4
	v_mov_b32_e32 v131, v4
	s_branch .LBB0_1978

.LBB0_1987:
	s_andn2_b64 vcc, exec, s[34:35]
	s_cbranch_vccnz .LBB0_1970
	s_add_i32 s50, s30, 0xffffee00
	s_lshl_b64 s[30:31], s[50:51], 2
	s_add_u32 s30, s54, s30
	s_addc_u32 s31, s55, s31
	v_lshlrev_b32_e32 v132, 5, v166
	v_or_b32_e32 v133, s46, v165
	v_lshl_add_u32 v146, v133, 2, s21
	ds_read2_b32 v[160:161], v146 offset1:16
	s_lshr_b32 s19, s50, 10
	s_lshl_b32 s21, s58, 2
	s_add_i32 s30, s19, s21
	s_lshl_b32 s34, s50, 8
	s_ashr_i32 s31, s30, 31
	s_and_b32 s19, s34, 0x30000
	s_lshl_b64 s[30:31], s[30:31], 18
	v_lshlrev_b32_e32 v134, 7, v166
	s_add_u32 s21, s0, s30
	v_and_b32_e32 v134, 0x100, v134
	s_waitcnt lgkmcnt(0)
	v_mul_f32_e32 v147, 0xbfb8aa3b, v160
	s_addc_u32 s31, s1, s31
	v_lshlrev_b32_e32 v2, 3, v166
	v_or_b32_e32 v134, s53, v134
	s_add_u32 s30, s21, s19
	v_and_b32_e32 v2, 8, v2
	v_add_lshl_u32 v134, v134, v133, 4
	s_addc_u32 s31, s31, 0
	v_ashrrev_i32_e32 v135, 31, v134
	v_lshl_add_u64 v[132:133], s[30:31], 0, v[2:3]
	v_lshl_add_u64 v[166:167], v[132:133], 0, v[134:135]
	s_mov_b32 s19, 0x8000
	v_mul_f32_e32 v144, 0xbfb8aa3b, v236
	v_mul_f32_e32 v142, 0xbfb8aa3b, v240
	v_mul_f32_e32 v145, 0xbfb8aa3b, v237
	v_mul_f32_e32 v140, 0xbfb8aa3b, v241
	v_fma_f32 v128, v128, v147, v144
	v_fma_f32 v124, v124, v147, v142
	v_mul_f32_e32 v143, 0xbfb8aa3b, v238
	v_mul_f32_e32 v138, 0xbfb8aa3b, v242
	v_fma_f32 v129, v129, v147, v145
	v_fma_f32 v125, v125, v147, v140
	v_exp_f32_e32 v128, v128
	v_exp_f32_e32 v124, v124
	v_mul_f32_e32 v141, 0xbfb8aa3b, v239
	v_mul_f32_e32 v139, 0xbfb8aa3b, v243
	v_fma_f32 v130, v130, v147, v143
	v_fma_f32 v126, v126, v147, v138
	v_exp_f32_e32 v129, v129
	v_exp_f32_e32 v125, v125
	v_mul_f32_e32 v137, 0xbfb8aa3b, v244
	v_mul_f32_e32 v135, 0xbfb8aa3b, v245
	v_fma_f32 v131, v131, v147, v141
	v_fma_f32 v127, v127, v147, v139
	v_exp_f32_e32 v130, v130
	v_exp_f32_e32 v126, v126
	v_fma_f32 v120, v120, v147, v137
	v_fma_f32 v121, v121, v147, v135
	v_exp_f32_e32 v131, v131
	v_exp_f32_e32 v127, v127
	v_mul_f32_e32 v136, 0xbfb8aa3b, v246
	v_exp_f32_e32 v120, v120
	v_exp_f32_e32 v121, v121
	v_fmamk_f32 v128, v128, 0x3b808081, v219
	v_fmamk_f32 v124, v124, 0x3b808081, v219
	v_fma_f32 v122, v122, v147, v136
	v_fmamk_f32 v129, v129, 0x3b808081, v219
	v_fmamk_f32 v125, v125, 0x3b808081, v219
	v_rcp_f32_e32 v128, v128
	v_rcp_f32_e32 v124, v124
	v_exp_f32_e32 v122, v122
	v_fmamk_f32 v130, v130, 0x3b808081, v219
	v_fmamk_f32 v126, v126, 0x3b808081, v219
	v_rcp_f32_e32 v129, v129
	v_rcp_f32_e32 v125, v125
	v_fmamk_f32 v131, v131, 0x3b808081, v219
	v_fmamk_f32 v127, v127, 0x3b808081, v219
	v_rcp_f32_e32 v130, v130
	v_rcp_f32_e32 v126, v126
	v_fmamk_f32 v120, v120, 0x3b808081, v219
	v_fmamk_f32 v121, v121, 0x3b808081, v219
	v_rcp_f32_e32 v131, v131
	v_rcp_f32_e32 v127, v127
	v_mul_f32_e32 v2, 0xbfb8aa3b, v247
	v_rcp_f32_e32 v160, v120
	v_rcp_f32_e32 v165, v121
	v_cvt_pk_u8_f32 v120, v128, 0, 0
	v_cvt_pk_u8_f32 v121, v124, 0, 0
	v_fma_f32 v123, v123, v147, v2
	v_fmamk_f32 v122, v122, 0x3b808081, v219
	v_cvt_pk_u8_f32 v120, v129, 1, v120
	v_cvt_pk_u8_f32 v121, v125, 1, v121
	v_exp_f32_e32 v123, v123
	v_rcp_f32_e32 v122, v122
	v_cvt_pk_u8_f32 v120, v130, 2, v120
	v_cvt_pk_u8_f32 v121, v126, 2, v121
	v_cvt_pk_u8_f32 v120, v131, 3, v120
	v_cvt_pk_u8_f32 v121, v127, 3, v121
	global_store_dwordx2 v[166:167], v[120:121], off
	v_cvt_pk_u8_f32 v120, v160, 0, 0
	v_cvt_pk_u8_f32 v120, v165, 1, v120
	v_cvt_pk_u8_f32 v121, v122, 2, v120
	v_fmamk_f32 v120, v123, 0x3b808081, v219
	v_rcp_f32_e32 v122, v120
	v_mul_f32_e32 v120, 0xbfb8aa3b, v248
	v_fma_f32 v116, v116, v147, v120
	v_exp_f32_e32 v123, v116
	v_mul_f32_e32 v116, 0xbfb8aa3b, v249
	v_fma_f32 v117, v117, v147, v116
	v_exp_f32_e32 v117, v117
	v_cvt_pk_u8_f32 v122, v122, 3, v121
	v_fmamk_f32 v121, v123, 0x3b808081, v219
	v_rcp_f32_e32 v121, v121
	v_fmamk_f32 v123, v117, 0x3b808081, v219
	v_mul_f32_e32 v117, 0xbfb8aa3b, v250
	v_fma_f32 v118, v118, v147, v117
	v_exp_f32_e32 v124, v118
	v_mul_f32_e32 v118, 0xbfb8aa3b, v251
	v_fma_f32 v119, v119, v147, v118
	v_exp_f32_e32 v119, v119
	v_rcp_f32_e32 v123, v123
	v_fmamk_f32 v124, v124, 0x3b808081, v219
	v_rcp_f32_e32 v124, v124
	v_fmamk_f32 v119, v119, 0x3b808081, v219
	v_rcp_f32_e32 v119, v119
	v_cvt_pk_u8_f32 v121, v121, 0, 0
	v_cvt_pk_u8_f32 v121, v123, 1, v121
	v_cvt_pk_u8_f32 v121, v124, 2, v121
	v_cvt_pk_u8_f32 v123, v119, 3, v121
	v_mul_f32_e32 v119, 0xbfb8aa3b, v161
	v_fma_f32 v104, v104, v119, v137
	v_exp_f32_e32 v104, v104
	v_fma_f32 v105, v105, v119, v135
	v_exp_f32_e32 v105, v105
	v_fma_f32 v106, v106, v119, v136
	v_exp_f32_e32 v106, v106
	v_fmamk_f32 v104, v104, 0x3b808081, v219
	v_rcp_f32_e32 v104, v104
	v_fmamk_f32 v105, v105, 0x3b808081, v219
	v_fma_f32 v107, v107, v119, v2
	v_rcp_f32_e32 v105, v105
	v_fmamk_f32 v106, v106, 0x3b808081, v219
	v_exp_f32_e32 v107, v107
	v_rcp_f32_e32 v106, v106
	v_cvt_pk_u8_f32 v104, v104, 0, 0
	v_cvt_pk_u8_f32 v104, v105, 1, v104
	v_fmamk_f32 v105, v107, 0x3b808081, v219
	v_fma_f32 v100, v100, v119, v120
	v_cvt_pk_u8_f32 v104, v106, 2, v104
	v_rcp_f32_e32 v105, v105
	v_exp_f32_e32 v106, v100
	v_fma_f32 v100, v101, v119, v116
	v_exp_f32_e32 v101, v100
	v_fma_f32 v102, v102, v119, v117
	v_exp_f32_e32 v102, v102
	v_fma_f32 v103, v103, v119, v118
	v_exp_f32_e32 v103, v103
	v_cvt_pk_u8_f32 v100, v105, 3, v104
	v_fmamk_f32 v104, v106, 0x3b808081, v219
	v_rcp_f32_e32 v104, v104
	v_fmamk_f32 v101, v101, 0x3b808081, v219
	v_rcp_f32_e32 v101, v101
	v_fmamk_f32 v102, v102, 0x3b808081, v219
	v_rcp_f32_e32 v102, v102
	v_fmamk_f32 v103, v103, 0x3b808081, v219
	v_rcp_f32_e32 v103, v103
	v_cvt_pk_u8_f32 v104, v104, 0, 0
	v_cvt_pk_u8_f32 v101, v101, 1, v104
	v_cvt_pk_u8_f32 v101, v102, 2, v101
	v_cvt_pk_u8_f32 v101, v103, 3, v101
	ds_read2_b32 v[102:103], v146 offset0:32 offset1:48
	v_fma_f32 v112, v112, v119, v144
	v_exp_f32_e32 v112, v112
	v_fma_f32 v113, v113, v119, v145
	v_exp_f32_e32 v113, v113
	s_waitcnt lgkmcnt(0)
	v_mul_f32_e32 v102, 0xbfb8aa3b, v102
	v_fma_f32 v88, v88, v102, v137
	v_exp_f32_e32 v88, v88
	v_fma_f32 v89, v89, v102, v135
	v_exp_f32_e32 v89, v89
	v_fma_f32 v90, v90, v102, v136
	v_exp_f32_e32 v90, v90
	v_fmamk_f32 v88, v88, 0x3b808081, v219
	v_fma_f32 v108, v108, v119, v142
	v_rcp_f32_e32 v88, v88
	v_fmamk_f32 v89, v89, 0x3b808081, v219
	v_fma_f32 v91, v91, v102, v2
	v_exp_f32_e32 v108, v108
	v_rcp_f32_e32 v89, v89
	v_fmamk_f32 v90, v90, 0x3b808081, v219
	v_exp_f32_e32 v91, v91
	v_add_co_u32_e32 v124, vcc, s19, v166
	v_rcp_f32_e32 v90, v90
	s_nop 0
	v_addc_co_u32_e32 v125, vcc, 0, v167, vcc
	v_fmamk_f32 v112, v112, 0x3b808081, v219
	global_store_dwordx2 v[124:125], v[122:123], off
	v_add_u32_e32 v122, 0x100, v134
	v_rcp_f32_e32 v121, v112
	v_fmamk_f32 v112, v113, 0x3b808081, v219
	v_cvt_pk_u8_f32 v88, v88, 0, 0
	v_ashrrev_i32_e32 v123, 31, v122
	v_rcp_f32_e32 v124, v112
	v_fma_f32 v112, v114, v119, v143
	v_fmamk_f32 v108, v108, 0x3b808081, v219
	v_cvt_pk_u8_f32 v88, v89, 1, v88
	v_fmamk_f32 v89, v91, 0x3b808081, v219
	v_fma_f32 v84, v84, v102, v120
	v_exp_f32_e32 v114, v112
	v_lshl_add_u64 v[112:113], v[132:133], 0, v[122:123]
	v_rcp_f32_e32 v122, v108
	v_fma_f32 v108, v109, v119, v140
	v_cvt_pk_u8_f32 v88, v90, 2, v88
	v_rcp_f32_e32 v89, v89
	v_exp_f32_e32 v90, v84
	v_fma_f32 v84, v85, v102, v116
	v_exp_f32_e32 v109, v108
	v_fma_f32 v110, v110, v119, v138
	v_exp_f32_e32 v85, v84
	v_fma_f32 v86, v86, v102, v117
	v_fma_f32 v115, v115, v119, v141
	v_exp_f32_e32 v110, v110
	v_fma_f32 v111, v111, v119, v139
	v_fma_f32 v96, v96, v102, v144
	v_exp_f32_e32 v86, v86
	v_fma_f32 v87, v87, v102, v118
	v_exp_f32_e32 v115, v115
	v_exp_f32_e32 v111, v111
	v_exp_f32_e32 v96, v96
	v_fma_f32 v97, v97, v102, v145
	v_exp_f32_e32 v87, v87
	v_fmamk_f32 v114, v114, 0x3b808081, v219
	v_exp_f32_e32 v97, v97
	v_cvt_pk_u8_f32 v84, v89, 3, v88
	v_fmamk_f32 v88, v90, 0x3b808081, v219
	v_rcp_f32_e32 v114, v114
	v_fmamk_f32 v109, v109, 0x3b808081, v219
	v_rcp_f32_e32 v88, v88
	v_fmamk_f32 v85, v85, 0x3b808081, v219
	v_rcp_f32_e32 v109, v109
	v_fmamk_f32 v110, v110, 0x3b808081, v219
	v_add_co_u32_e32 v104, vcc, s19, v112
	v_rcp_f32_e32 v85, v85
	v_fmamk_f32 v86, v86, 0x3b808081, v219
	v_cvt_pk_u8_f32 v121, v121, 0, 0
	v_fmamk_f32 v115, v115, 0x3b808081, v219
	v_rcp_f32_e32 v110, v110
	v_fmamk_f32 v111, v111, 0x3b808081, v219
	v_addc_co_u32_e32 v105, vcc, 0, v113, vcc
	v_fmamk_f32 v96, v96, 0x3b808081, v219
	v_rcp_f32_e32 v86, v86
	v_fmamk_f32 v87, v87, 0x3b808081, v219
	v_cvt_pk_u8_f32 v121, v124, 1, v121
	v_rcp_f32_e32 v115, v115
	v_rcp_f32_e32 v111, v111
	global_store_dwordx2 v[104:105], v[100:101], off
	v_add_u32_e32 v100, 0x200, v134
	v_rcp_f32_e32 v104, v96
	v_fmamk_f32 v96, v97, 0x3b808081, v219
	v_rcp_f32_e32 v87, v87
	v_cvt_pk_u8_f32 v108, v114, 2, v121
	v_cvt_pk_u8_f32 v114, v122, 0, 0
	v_ashrrev_i32_e32 v101, 31, v100
	v_rcp_f32_e32 v105, v96
	v_fma_f32 v96, v98, v102, v143
	v_cvt_pk_u8_f32 v88, v88, 0, 0
	v_cvt_pk_u8_f32 v109, v109, 1, v114
	v_exp_f32_e32 v98, v96
	v_lshl_add_u64 v[96:97], v[132:133], 0, v[100:101]
	v_cvt_pk_u8_f32 v85, v85, 1, v88
	v_cvt_pk_u8_f32 v109, v110, 2, v109
	v_cvt_pk_u8_f32 v85, v86, 2, v85
	v_add_co_u32_e32 v86, vcc, s19, v96
	v_cvt_pk_u8_f32 v108, v115, 3, v108
	v_cvt_pk_u8_f32 v109, v111, 3, v109
	v_cvt_pk_u8_f32 v85, v87, 3, v85
	v_addc_co_u32_e32 v87, vcc, 0, v97, vcc
	global_store_dwordx2 v[112:113], v[108:109], off
	global_store_dwordx2 v[86:87], v[84:85], off
	v_mul_f32_e32 v86, 0xbfb8aa3b, v103
	v_fma_f32 v72, v72, v86, v137
	v_exp_f32_e32 v72, v72
	v_fma_f32 v73, v73, v86, v135
	v_exp_f32_e32 v73, v73
	v_fma_f32 v74, v74, v86, v136
	v_exp_f32_e32 v74, v74
	v_fmamk_f32 v72, v72, 0x3b808081, v219
	v_rcp_f32_e32 v72, v72
	v_fmamk_f32 v73, v73, 0x3b808081, v219
	v_fma_f32 v75, v75, v86, v2
	v_rcp_f32_e32 v73, v73
	v_fmamk_f32 v74, v74, 0x3b808081, v219
	v_exp_f32_e32 v75, v75
	v_rcp_f32_e32 v74, v74
	v_cvt_pk_u8_f32 v72, v72, 0, 0
	v_cvt_pk_u8_f32 v72, v73, 1, v72
	v_fmamk_f32 v73, v75, 0x3b808081, v219
	v_fma_f32 v68, v68, v86, v120
	v_cvt_pk_u8_f32 v72, v74, 2, v72
	v_rcp_f32_e32 v73, v73
	v_exp_f32_e32 v74, v68
	v_fma_f32 v68, v69, v86, v116
	v_exp_f32_e32 v69, v68
	v_fma_f32 v70, v70, v86, v117
	v_exp_f32_e32 v70, v70
	v_fma_f32 v71, v71, v86, v118
	v_exp_f32_e32 v71, v71
	v_cvt_pk_u8_f32 v68, v73, 3, v72
	v_fmamk_f32 v72, v74, 0x3b808081, v219
	v_rcp_f32_e32 v72, v72
	v_fmamk_f32 v69, v69, 0x3b808081, v219
	v_rcp_f32_e32 v69, v69
	v_fmamk_f32 v70, v70, 0x3b808081, v219
	v_rcp_f32_e32 v70, v70
	v_fmamk_f32 v71, v71, 0x3b808081, v219
	v_rcp_f32_e32 v71, v71
	v_cvt_pk_u8_f32 v72, v72, 0, 0
	v_cvt_pk_u8_f32 v69, v69, 1, v72
	v_cvt_pk_u8_f32 v69, v70, 2, v69
	v_cvt_pk_u8_f32 v69, v71, 3, v69
	ds_read2_b32 v[70:71], v146 offset0:128 offset1:144
	v_fma_f32 v92, v92, v102, v142
	v_exp_f32_e32 v92, v92
	v_fma_f32 v80, v80, v86, v144
	v_exp_f32_e32 v80, v80
	s_waitcnt lgkmcnt(0)
	v_mul_f32_e32 v70, 0xbfb8aa3b, v70
	v_fma_f32 v56, v56, v70, v137
	v_exp_f32_e32 v56, v56
	v_fma_f32 v57, v57, v70, v135
	v_exp_f32_e32 v57, v57
	v_fma_f32 v58, v58, v70, v136
	v_exp_f32_e32 v58, v58
	v_fma_f32 v81, v81, v86, v145
	v_fmamk_f32 v56, v56, 0x3b808081, v219
	v_fmamk_f32 v92, v92, 0x3b808081, v219
	v_exp_f32_e32 v81, v81
	v_fma_f32 v76, v76, v86, v142
	v_rcp_f32_e32 v56, v56
	v_fmamk_f32 v57, v57, 0x3b808081, v219
	v_fma_f32 v59, v59, v70, v2
	v_rcp_f32_e32 v101, v92
	v_fma_f32 v92, v93, v102, v140
	v_exp_f32_e32 v76, v76
	v_rcp_f32_e32 v57, v57
	v_fmamk_f32 v58, v58, 0x3b808081, v219
	v_exp_f32_e32 v59, v59
	v_exp_f32_e32 v93, v92
	v_fma_f32 v94, v94, v102, v138
	v_rcp_f32_e32 v58, v58
	v_fma_f32 v99, v99, v102, v141
	v_exp_f32_e32 v94, v94
	v_fma_f32 v95, v95, v102, v139
	v_fmamk_f32 v80, v80, 0x3b808081, v219
	v_exp_f32_e32 v99, v99
	v_exp_f32_e32 v95, v95
	v_add_u32_e32 v84, 0x300, v134
	v_rcp_f32_e32 v87, v80
	v_fmamk_f32 v80, v81, 0x3b808081, v219
	v_cvt_pk_u8_f32 v56, v56, 0, 0
	v_fmamk_f32 v98, v98, 0x3b808081, v219
	v_ashrrev_i32_e32 v85, 31, v84
	v_rcp_f32_e32 v88, v80
	v_fma_f32 v80, v82, v86, v143
	v_fmamk_f32 v76, v76, 0x3b808081, v219
	v_cvt_pk_u8_f32 v56, v57, 1, v56
	v_fmamk_f32 v57, v59, 0x3b808081, v219
	v_fma_f32 v52, v52, v70, v120
	v_rcp_f32_e32 v98, v98
	v_fmamk_f32 v93, v93, 0x3b808081, v219
	v_exp_f32_e32 v82, v80
	v_lshl_add_u64 v[80:81], v[132:133], 0, v[84:85]
	v_rcp_f32_e32 v85, v76
	v_fma_f32 v76, v77, v86, v140
	v_cvt_pk_u8_f32 v56, v58, 2, v56
	v_rcp_f32_e32 v57, v57
	v_exp_f32_e32 v58, v52
	v_fma_f32 v52, v53, v70, v116
	v_rcp_f32_e32 v93, v93
	v_fmamk_f32 v94, v94, 0x3b808081, v219
	v_exp_f32_e32 v77, v76
	v_fma_f32 v78, v78, v86, v138
	v_exp_f32_e32 v53, v52
	v_fma_f32 v54, v54, v70, v117
	v_cvt_pk_u8_f32 v100, v104, 0, 0
	v_fmamk_f32 v99, v99, 0x3b808081, v219
	v_rcp_f32_e32 v94, v94
	v_fmamk_f32 v95, v95, 0x3b808081, v219
	v_fma_f32 v83, v83, v86, v141
	v_exp_f32_e32 v78, v78
	v_fma_f32 v79, v79, v86, v139
	v_fma_f32 v64, v64, v70, v144
	v_exp_f32_e32 v54, v54
	v_fma_f32 v55, v55, v70, v118
	v_cvt_pk_u8_f32 v100, v105, 1, v100
	v_rcp_f32_e32 v99, v99
	v_rcp_f32_e32 v95, v95
	v_exp_f32_e32 v83, v83
	v_exp_f32_e32 v79, v79
	v_exp_f32_e32 v64, v64
	v_fma_f32 v65, v65, v70, v145
	v_exp_f32_e32 v55, v55
	v_cvt_pk_u8_f32 v92, v98, 2, v100
	v_cvt_pk_u8_f32 v98, v101, 0, 0
	v_fmamk_f32 v82, v82, 0x3b808081, v219
	v_exp_f32_e32 v65, v65
	v_cvt_pk_u8_f32 v52, v57, 3, v56
	v_fmamk_f32 v56, v58, 0x3b808081, v219
	v_cvt_pk_u8_f32 v93, v93, 1, v98
	v_rcp_f32_e32 v82, v82
	v_fmamk_f32 v77, v77, 0x3b808081, v219
	v_rcp_f32_e32 v56, v56
	v_fmamk_f32 v53, v53, 0x3b808081, v219
	v_cvt_pk_u8_f32 v93, v94, 2, v93
	v_rcp_f32_e32 v77, v77
	v_fmamk_f32 v78, v78, 0x3b808081, v219
	v_add_co_u32_e32 v72, vcc, s19, v80
	v_rcp_f32_e32 v53, v53
	v_fmamk_f32 v54, v54, 0x3b808081, v219
	v_cvt_pk_u8_f32 v92, v99, 3, v92
	v_cvt_pk_u8_f32 v93, v95, 3, v93
	v_cvt_pk_u8_f32 v84, v87, 0, 0
	v_fmamk_f32 v83, v83, 0x3b808081, v219
	v_rcp_f32_e32 v78, v78
	v_fmamk_f32 v79, v79, 0x3b808081, v219
	v_addc_co_u32_e32 v73, vcc, 0, v81, vcc
	v_fmamk_f32 v64, v64, 0x3b808081, v219
	v_rcp_f32_e32 v54, v54
	v_fmamk_f32 v55, v55, 0x3b808081, v219
	global_store_dwordx2 v[96:97], v[92:93], off
	v_cvt_pk_u8_f32 v84, v88, 1, v84
	v_rcp_f32_e32 v83, v83
	v_rcp_f32_e32 v79, v79
	global_store_dwordx2 v[72:73], v[68:69], off
	v_add_u32_e32 v68, 0x800, v134
	v_rcp_f32_e32 v72, v64
	v_fmamk_f32 v64, v65, 0x3b808081, v219
	v_rcp_f32_e32 v55, v55
	v_cvt_pk_u8_f32 v76, v82, 2, v84
	v_cvt_pk_u8_f32 v82, v85, 0, 0
	v_ashrrev_i32_e32 v69, 31, v68
	v_rcp_f32_e32 v73, v64
	v_fma_f32 v64, v66, v70, v143
	v_cvt_pk_u8_f32 v56, v56, 0, 0
	v_cvt_pk_u8_f32 v77, v77, 1, v82
	v_exp_f32_e32 v66, v64
	v_lshl_add_u64 v[64:65], v[132:133], 0, v[68:69]
	v_cvt_pk_u8_f32 v53, v53, 1, v56
	v_cvt_pk_u8_f32 v77, v78, 2, v77
	v_cvt_pk_u8_f32 v53, v54, 2, v53
	v_add_co_u32_e32 v54, vcc, s19, v64
	v_cvt_pk_u8_f32 v76, v83, 3, v76
	v_cvt_pk_u8_f32 v77, v79, 3, v77
	v_cvt_pk_u8_f32 v53, v55, 3, v53
	v_addc_co_u32_e32 v55, vcc, 0, v65, vcc
	global_store_dwordx2 v[80:81], v[76:77], off
	global_store_dwordx2 v[54:55], v[52:53], off
	v_mul_f32_e32 v54, 0xbfb8aa3b, v71
	v_fma_f32 v40, v40, v54, v137
	v_exp_f32_e32 v40, v40
	v_fma_f32 v41, v41, v54, v135
	v_exp_f32_e32 v41, v41
	v_fma_f32 v42, v42, v54, v136
	v_exp_f32_e32 v42, v42
	v_fmamk_f32 v40, v40, 0x3b808081, v219
	v_rcp_f32_e32 v40, v40
	v_fmamk_f32 v41, v41, 0x3b808081, v219
	v_fma_f32 v43, v43, v54, v2
	v_rcp_f32_e32 v41, v41
	v_fmamk_f32 v42, v42, 0x3b808081, v219
	v_exp_f32_e32 v43, v43
	v_rcp_f32_e32 v42, v42
	v_cvt_pk_u8_f32 v40, v40, 0, 0
	v_cvt_pk_u8_f32 v40, v41, 1, v40
	v_fmamk_f32 v41, v43, 0x3b808081, v219
	v_fma_f32 v36, v36, v54, v120
	v_cvt_pk_u8_f32 v40, v42, 2, v40
	v_rcp_f32_e32 v41, v41
	v_exp_f32_e32 v42, v36
	v_fma_f32 v36, v37, v54, v116
	v_exp_f32_e32 v37, v36
	v_fma_f32 v38, v38, v54, v117
	v_exp_f32_e32 v38, v38
	v_fma_f32 v39, v39, v54, v118
	v_exp_f32_e32 v39, v39
	v_cvt_pk_u8_f32 v36, v41, 3, v40
	v_fmamk_f32 v40, v42, 0x3b808081, v219
	v_rcp_f32_e32 v40, v40
	v_fmamk_f32 v37, v37, 0x3b808081, v219
	v_rcp_f32_e32 v37, v37
	v_fmamk_f32 v38, v38, 0x3b808081, v219
	v_rcp_f32_e32 v38, v38
	v_fmamk_f32 v39, v39, 0x3b808081, v219
	v_rcp_f32_e32 v39, v39
	v_cvt_pk_u8_f32 v40, v40, 0, 0
	v_cvt_pk_u8_f32 v37, v37, 1, v40
	v_cvt_pk_u8_f32 v37, v38, 2, v37
	v_cvt_pk_u8_f32 v37, v39, 3, v37
	ds_read2_b32 v[38:39], v146 offset0:160 offset1:176
	v_fma_f32 v60, v60, v70, v142
	v_exp_f32_e32 v60, v60
	v_fma_f32 v48, v48, v54, v144
	v_exp_f32_e32 v48, v48
	s_waitcnt lgkmcnt(0)
	v_mul_f32_e32 v38, 0xbfb8aa3b, v38
	v_fma_f32 v24, v24, v38, v137
	v_exp_f32_e32 v24, v24
	v_fma_f32 v25, v25, v38, v135
	v_exp_f32_e32 v25, v25
	v_fma_f32 v26, v26, v38, v136
	v_exp_f32_e32 v26, v26
	v_fma_f32 v49, v49, v54, v145
	v_fmamk_f32 v24, v24, 0x3b808081, v219
	v_fmamk_f32 v60, v60, 0x3b808081, v219
	v_exp_f32_e32 v49, v49
	v_fma_f32 v44, v44, v54, v142
	v_rcp_f32_e32 v24, v24
	v_fmamk_f32 v25, v25, 0x3b808081, v219
	v_fma_f32 v27, v27, v38, v2
	v_rcp_f32_e32 v69, v60
	v_fma_f32 v60, v61, v70, v140
	v_exp_f32_e32 v44, v44
	v_rcp_f32_e32 v25, v25
	v_fmamk_f32 v26, v26, 0x3b808081, v219
	v_exp_f32_e32 v27, v27
	v_exp_f32_e32 v61, v60
	v_fma_f32 v62, v62, v70, v138
	v_rcp_f32_e32 v26, v26
	v_fma_f32 v67, v67, v70, v141
	v_exp_f32_e32 v62, v62
	v_fma_f32 v63, v63, v70, v139
	v_fmamk_f32 v48, v48, 0x3b808081, v219
	v_exp_f32_e32 v67, v67
	v_exp_f32_e32 v63, v63
	v_add_u32_e32 v52, 0x900, v134
	v_rcp_f32_e32 v55, v48
	v_fmamk_f32 v48, v49, 0x3b808081, v219
	v_cvt_pk_u8_f32 v24, v24, 0, 0
	v_fmamk_f32 v66, v66, 0x3b808081, v219
	v_ashrrev_i32_e32 v53, 31, v52
	v_rcp_f32_e32 v56, v48
	v_fma_f32 v48, v50, v54, v143
	v_fmamk_f32 v44, v44, 0x3b808081, v219
	v_cvt_pk_u8_f32 v24, v25, 1, v24
	v_fmamk_f32 v25, v27, 0x3b808081, v219
	v_fma_f32 v20, v20, v38, v120
	v_rcp_f32_e32 v66, v66
	v_fmamk_f32 v61, v61, 0x3b808081, v219
	v_exp_f32_e32 v50, v48
	v_lshl_add_u64 v[48:49], v[132:133], 0, v[52:53]
	v_rcp_f32_e32 v53, v44
	v_fma_f32 v44, v45, v54, v140
	v_cvt_pk_u8_f32 v24, v26, 2, v24
	v_rcp_f32_e32 v25, v25
	v_exp_f32_e32 v26, v20
	v_fma_f32 v20, v21, v38, v116
	v_rcp_f32_e32 v61, v61
	v_fmamk_f32 v62, v62, 0x3b808081, v219
	v_exp_f32_e32 v45, v44
	v_fma_f32 v46, v46, v54, v138
	v_exp_f32_e32 v21, v20
	v_fma_f32 v22, v22, v38, v117
	v_cvt_pk_u8_f32 v68, v72, 0, 0
	v_fmamk_f32 v67, v67, 0x3b808081, v219
	v_rcp_f32_e32 v62, v62
	v_fmamk_f32 v63, v63, 0x3b808081, v219
	v_fma_f32 v51, v51, v54, v141
	v_exp_f32_e32 v46, v46
	v_fma_f32 v47, v47, v54, v139
	v_fma_f32 v32, v32, v38, v144
	v_exp_f32_e32 v22, v22
	v_fma_f32 v23, v23, v38, v118
	v_cvt_pk_u8_f32 v68, v73, 1, v68
	v_rcp_f32_e32 v67, v67
	v_rcp_f32_e32 v63, v63
	v_exp_f32_e32 v51, v51
	v_exp_f32_e32 v47, v47
	v_exp_f32_e32 v32, v32
	v_fma_f32 v33, v33, v38, v145
	v_exp_f32_e32 v23, v23
	v_cvt_pk_u8_f32 v60, v66, 2, v68
	v_cvt_pk_u8_f32 v66, v69, 0, 0
	v_fmamk_f32 v50, v50, 0x3b808081, v219
	v_exp_f32_e32 v33, v33
	v_cvt_pk_u8_f32 v20, v25, 3, v24
	v_fmamk_f32 v24, v26, 0x3b808081, v219
	v_cvt_pk_u8_f32 v61, v61, 1, v66
	v_rcp_f32_e32 v50, v50
	v_fmamk_f32 v45, v45, 0x3b808081, v219
	v_rcp_f32_e32 v24, v24
	v_fmamk_f32 v21, v21, 0x3b808081, v219
	v_cvt_pk_u8_f32 v61, v62, 2, v61
	v_rcp_f32_e32 v45, v45
	v_fmamk_f32 v46, v46, 0x3b808081, v219
	v_add_co_u32_e32 v40, vcc, s19, v48
	v_rcp_f32_e32 v21, v21
	v_fmamk_f32 v22, v22, 0x3b808081, v219
	v_cvt_pk_u8_f32 v60, v67, 3, v60
	v_cvt_pk_u8_f32 v61, v63, 3, v61
	v_cvt_pk_u8_f32 v52, v55, 0, 0
	v_fmamk_f32 v51, v51, 0x3b808081, v219
	v_rcp_f32_e32 v46, v46
	v_fmamk_f32 v47, v47, 0x3b808081, v219
	v_addc_co_u32_e32 v41, vcc, 0, v49, vcc
	v_fmamk_f32 v32, v32, 0x3b808081, v219
	v_rcp_f32_e32 v22, v22
	v_fmamk_f32 v23, v23, 0x3b808081, v219
	global_store_dwordx2 v[64:65], v[60:61], off
	v_cvt_pk_u8_f32 v52, v56, 1, v52
	v_rcp_f32_e32 v51, v51
	v_rcp_f32_e32 v47, v47
	global_store_dwordx2 v[40:41], v[36:37], off
	v_add_u32_e32 v36, 0xa00, v134
	v_rcp_f32_e32 v40, v32
	v_fmamk_f32 v32, v33, 0x3b808081, v219
	v_rcp_f32_e32 v23, v23
	v_cvt_pk_u8_f32 v44, v50, 2, v52
	v_cvt_pk_u8_f32 v50, v53, 0, 0
	v_ashrrev_i32_e32 v37, 31, v36
	v_rcp_f32_e32 v41, v32
	v_fma_f32 v32, v34, v38, v143
	v_cvt_pk_u8_f32 v24, v24, 0, 0
	v_cvt_pk_u8_f32 v45, v45, 1, v50
	v_exp_f32_e32 v34, v32
	v_lshl_add_u64 v[32:33], v[132:133], 0, v[36:37]
	v_cvt_pk_u8_f32 v21, v21, 1, v24
	v_cvt_pk_u8_f32 v45, v46, 2, v45
	v_cvt_pk_u8_f32 v21, v22, 2, v21
	v_add_co_u32_e32 v22, vcc, s19, v32
	v_cvt_pk_u8_f32 v44, v51, 3, v44
	v_cvt_pk_u8_f32 v45, v47, 3, v45
	v_cvt_pk_u8_f32 v21, v23, 3, v21
	v_addc_co_u32_e32 v23, vcc, 0, v33, vcc
	global_store_dwordx2 v[48:49], v[44:45], off
	global_store_dwordx2 v[22:23], v[20:21], off
	v_mul_f32_e32 v22, 0xbfb8aa3b, v39
	v_fmac_f32_e32 v137, v8, v22
	v_exp_f32_e32 v8, v137
	v_fmac_f32_e32 v135, v9, v22
	v_exp_f32_e32 v9, v135
	v_fmac_f32_e32 v136, v10, v22
	v_fma_f32 v28, v28, v38, v142
	v_fmamk_f32 v8, v8, 0x3b808081, v219
	v_exp_f32_e32 v10, v136
	v_fmac_f32_e32 v2, v11, v22
	v_exp_f32_e32 v28, v28
	v_rcp_f32_e32 v8, v8
	v_fmamk_f32 v9, v9, 0x3b808081, v219
	v_exp_f32_e32 v2, v2
	v_rcp_f32_e32 v9, v9
	v_fmac_f32_e32 v144, v16, v22
	v_exp_f32_e32 v16, v144
	v_fmac_f32_e32 v145, v17, v22
	v_fmamk_f32 v10, v10, 0x3b808081, v219
	v_fmamk_f32 v28, v28, 0x3b808081, v219
	v_exp_f32_e32 v17, v145
	v_fmac_f32_e32 v143, v18, v22
	v_fmac_f32_e32 v142, v12, v22
	v_rcp_f32_e32 v10, v10
	v_cvt_pk_u8_f32 v8, v8, 0, 0
	v_fmamk_f32 v2, v2, 0x3b808081, v219
	v_fmac_f32_e32 v120, v4, v22
	v_rcp_f32_e32 v37, v28
	v_fma_f32 v28, v29, v38, v140
	v_exp_f32_e32 v18, v143
	v_exp_f32_e32 v12, v142
	v_fmac_f32_e32 v140, v13, v22
	v_cvt_pk_u8_f32 v8, v9, 1, v8
	v_rcp_f32_e32 v2, v2
	v_exp_f32_e32 v9, v120
	v_fmac_f32_e32 v116, v5, v22
	v_exp_f32_e32 v29, v28
	v_fma_f32 v30, v30, v38, v138
	v_exp_f32_e32 v13, v140
	v_fmac_f32_e32 v138, v14, v22
	v_exp_f32_e32 v5, v116
	v_fmac_f32_e32 v117, v6, v22
	v_fma_f32 v35, v35, v38, v141
	v_exp_f32_e32 v30, v30
	v_fma_f32 v31, v31, v38, v139
	v_fmamk_f32 v16, v16, 0x3b808081, v219
	v_fmac_f32_e32 v141, v19, v22
	v_exp_f32_e32 v14, v138
	v_fmac_f32_e32 v139, v15, v22
	v_exp_f32_e32 v6, v117
	v_fmac_f32_e32 v118, v7, v22
	v_exp_f32_e32 v35, v35
	v_exp_f32_e32 v31, v31
	v_add_u32_e32 v20, 0xb00, v134
	v_rcp_f32_e32 v23, v16
	v_fmamk_f32 v16, v17, 0x3b808081, v219
	v_exp_f32_e32 v19, v141
	v_exp_f32_e32 v15, v139
	v_cvt_pk_u8_f32 v8, v10, 2, v8
	v_exp_f32_e32 v7, v118
	v_fmamk_f32 v34, v34, 0x3b808081, v219
	v_ashrrev_i32_e32 v21, 31, v20
	v_rcp_f32_e32 v24, v16
	v_fmamk_f32 v18, v18, 0x3b808081, v219
	v_fmamk_f32 v12, v12, 0x3b808081, v219
	v_cvt_pk_u8_f32 v4, v2, 3, v8
	v_fmamk_f32 v2, v9, 0x3b808081, v219
	v_rcp_f32_e32 v34, v34
	v_fmamk_f32 v29, v29, 0x3b808081, v219
	v_lshl_add_u64 v[16:17], v[132:133], 0, v[20:21]
	v_rcp_f32_e32 v18, v18
	v_rcp_f32_e32 v21, v12
	v_fmamk_f32 v13, v13, 0x3b808081, v219
	v_rcp_f32_e32 v2, v2
	v_fmamk_f32 v5, v5, 0x3b808081, v219
	v_rcp_f32_e32 v29, v29
	v_fmamk_f32 v30, v30, 0x3b808081, v219
	v_rcp_f32_e32 v13, v13
	v_fmamk_f32 v14, v14, 0x3b808081, v219
	v_rcp_f32_e32 v5, v5
	v_fmamk_f32 v6, v6, 0x3b808081, v219
	v_cvt_pk_u8_f32 v36, v40, 0, 0
	v_fmamk_f32 v35, v35, 0x3b808081, v219
	v_rcp_f32_e32 v30, v30
	v_fmamk_f32 v31, v31, 0x3b808081, v219
	v_cvt_pk_u8_f32 v20, v23, 0, 0
	v_fmamk_f32 v19, v19, 0x3b808081, v219
	v_rcp_f32_e32 v14, v14
	v_fmamk_f32 v15, v15, 0x3b808081, v219
	v_rcp_f32_e32 v6, v6
	v_fmamk_f32 v7, v7, 0x3b808081, v219
	v_cvt_pk_u8_f32 v36, v41, 1, v36
	v_rcp_f32_e32 v35, v35
	v_rcp_f32_e32 v31, v31
	v_cvt_pk_u8_f32 v20, v24, 1, v20
	v_rcp_f32_e32 v19, v19
	v_rcp_f32_e32 v15, v15
	v_rcp_f32_e32 v7, v7
	v_cvt_pk_u8_f32 v28, v34, 2, v36
	v_cvt_pk_u8_f32 v34, v37, 0, 0
	v_cvt_pk_u8_f32 v12, v18, 2, v20
	v_cvt_pk_u8_f32 v18, v21, 0, 0
	v_cvt_pk_u8_f32 v2, v2, 0, 0
	v_cvt_pk_u8_f32 v29, v29, 1, v34
	v_cvt_pk_u8_f32 v13, v13, 1, v18
	v_cvt_pk_u8_f32 v2, v5, 1, v2
	v_cvt_pk_u8_f32 v29, v30, 2, v29
	v_cvt_pk_u8_f32 v13, v14, 2, v13
	v_cvt_pk_u8_f32 v2, v6, 2, v2
	v_add_co_u32_e32 v6, vcc, 0x8000, v16
	v_cvt_pk_u8_f32 v28, v35, 3, v28
	v_cvt_pk_u8_f32 v29, v31, 3, v29
	v_cvt_pk_u8_f32 v12, v19, 3, v12
	v_cvt_pk_u8_f32 v13, v15, 3, v13
	v_cvt_pk_u8_f32 v5, v7, 3, v2
	v_addc_co_u32_e32 v7, vcc, 0, v17, vcc
	global_store_dwordx2 v[32:33], v[28:29], off
	global_store_dwordx2 v[16:17], v[12:13], off
	global_store_dwordx2 v[6:7], v[4:5], off
	s_branch .LBB0_1970
